# speedup vs baseline: 1.0454x; 1.0163x over previous
.LBB0_118:
	s_or_b64 exec, exec, s[60:61]
	s_setprio 0
	v_readfirstlane_b32 s74, v0
	v_mov_b32_e32 v42, 0
	v_mov_b32_e32 v50, 0
	v_bfe_u32 v36, v0, 6, 2
	v_lshl_or_b32 v44, v36, 13, v86
	v_mov_b32_e32 v45, 0
	v_lshl_add_u64 v[18:19], s[56:57], 0, v[44:45]
	v_add_co_u32_e32 v34, vcc, 0x1000, v18
	global_load_dwordx4 v[2:5], v44, s[56:57]
	global_load_dwordx4 v[6:9], v44, s[56:57] offset:1024
	global_load_dwordx4 v[10:13], v44, s[56:57] offset:2048
	global_load_dwordx4 v[14:17], v44, s[56:57] offset:3072
	v_addc_co_u32_e32 v35, vcc, 0, v19, vcc
	v_lshlrev_b32_e32 v44, 7, v36
	global_load_dwordx4 v[18:21], v[34:35], off
	global_load_dwordx4 v[22:25], v[34:35], off offset:1024
	global_load_dwordx4 v[26:29], v[34:35], off offset:2048
	global_load_dwordx4 v[30:33], v[34:35], off offset:3072
	v_lshl_add_u64 v[34:35], s[52:53], 0, v[44:45]
	v_lshlrev_b32_e32 v36, 2, v1
	v_mov_b32_e32 v37, v45
	v_lshl_add_u64 v[46:47], v[34:35], 0, v[36:37]
	global_load_dwordx4 v[34:37], v[46:47], off offset:16
	global_load_dwordx4 v[38:41], v[46:47], off
	v_add3_u32 v46, s66, v50, v79
	v_ashrrev_i32_e32 v47, 31, v46
	v_and_b32_e32 v0, 48, v0
	v_lshlrev_b64 v[46:47], 9, v[46:47]
	v_lshlrev_b32_e32 v0, 1, v0
	v_or3_b32 v46, v46, v44, v0
	v_mul_u32_u24_e32 v43, 0x110, v79
	s_movk_i32 s0, 0x1100
	v_lshl_add_u64 v[0:1], s[54:55], 0, v[46:47]
	v_mad_u32_u24 v42, v42, s0, v43
	s_mov_b32 s0, 0x10000
	v_lshl_add_u64 v[0:1], v[0:1], 0, 16
	v_add3_u32 v51, v42, v70, s0
	s_lshr_b32 s74, s74, 6
	s_and_b32 s74, s74, 3
	s_lshl_b32 s75, s74, 2
	s_add_i32 s75, s75, 0x26d50
	s_add_i32 s76, s33, 15
	s_lshr_b32 s76, s76, 4
	v_mov_b64_e32 v[60:61], v[0:1]
	v_mov_b32_e32 v62, v51
	s_mov_b32 s96, 1
